# attention stagger groups by wave>=4 (SIMD partners) instead of wave parity
# speedup vs baseline: 1.0113x; 1.0113x over previous
.LBB0_467:
	s_andn2_b64 vcc, exec, s[2:3]
	s_cbranch_vccnz .LBB0_607
	s_lshl_b32 s0, s75, 5
	s_lshl_b32 s10, s75, 10
	v_writelane_b32 v254, s0, 43
	s_lshl_b32 s0, s75, 4
	s_add_i32 s79, s10, s91
	v_writelane_b32 v254, s0, 45
	s_add_i32 s80, s79, 0x2000
	s_add_i32 s81, s79, 0x4000
	s_add_i32 s82, s79, 0x6000
	s_add_i32 s83, s79, 0x8000
	s_add_i32 s84, s79, 0xa000
	v_readlane_b32 s0, v254, 42
	s_cmp_eq_u32 s0, 1
	s_mov_b64 s[2:3], -1
	s_cbranch_scc1 .LBB0_564
	v_writelane_b32 v254, s10, 47
	v_writelane_b32 v254, s75, 48
	v_mbcnt_lo_u32_b32 v0, -1, 0
	v_mbcnt_hi_u32_b32 v0, -1, v0
	s_load_dwordx8 s[4:11], s[14:15], 0x60
	v_readlane_b32 s0, v254, 30
	v_readlane_b32 s1, v254, 31
	s_and_b64 s[0:1], s[0:1], exec
	s_movk_i32 s0, 0x400
	s_cselect_b32 s2, s0, 0x440
	s_cselect_b32 s0, 64, 0
	v_and_or_b32 v0, v0, 63, s0
	v_lshlrev_b32_e32 v2, 2, v0
	s_waitcnt lgkmcnt(0)
	global_load_dword v0, v2, s[4:5]
	global_load_dword v1, v2, s[6:7]
	v_readlane_b32 s1, v254, 37
	v_writelane_b32 v254, s2, 49
	s_cmp_ge_i32 s1, s2
	v_readlane_b32 s77, v254, 41
	s_waitcnt vmcnt(0)
	v_mul_f32_e32 v3, v0, v1
	ds_swizzle_b32 v3, v3 offset:swizzle(SWAP,1)
	s_waitcnt lgkmcnt(0)
	v_fmac_f32_e32 v3, v0, v1
	ds_swizzle_b32 v0, v3 offset:swizzle(SWAP,2)
	s_waitcnt lgkmcnt(0)
	v_add_f32_e32 v0, v3, v0
	global_load_dword v3, v2, s[8:9]
	s_nop 0
	global_load_dword v2, v2, s[10:11]
	ds_swizzle_b32 v1, v0 offset:swizzle(SWAP,4)
	s_waitcnt lgkmcnt(0)
	v_add_f32_e32 v0, v0, v1
	ds_swizzle_b32 v1, v0 offset:swizzle(SWAP,8)
	s_waitcnt lgkmcnt(0)
	v_add_f32_e32 v0, v0, v1
	ds_swizzle_b32 v1, v0 offset:swizzle(SWAP,16)
	s_waitcnt lgkmcnt(0)
	v_add_f32_e32 v0, v0, v1
	v_mov_b32_e32 v1, v0
	s_nop 1
	v_permlane32_swap_b32_e32 v0, v1
	s_waitcnt vmcnt(0)
	v_mul_f32_e32 v4, v3, v2
	ds_swizzle_b32 v4, v4 offset:swizzle(SWAP,1)
	s_waitcnt lgkmcnt(0)
	v_fmac_f32_e32 v4, v3, v2
	ds_swizzle_b32 v2, v4 offset:swizzle(SWAP,2)
	s_waitcnt lgkmcnt(0)
	v_add_f32_e32 v2, v4, v2
	ds_swizzle_b32 v3, v2 offset:swizzle(SWAP,4)
	s_waitcnt lgkmcnt(0)
	v_add_f32_e32 v2, v2, v3
	ds_swizzle_b32 v3, v2 offset:swizzle(SWAP,8)
	s_waitcnt lgkmcnt(0)
	v_add_f32_e32 v2, v2, v3
	ds_swizzle_b32 v3, v2 offset:swizzle(SWAP,16)
	s_waitcnt lgkmcnt(0)
	v_add_f32_e32 v2, v2, v3
	v_mov_b32_e32 v3, v2
	s_nop 1
	v_permlane32_swap_b32_e32 v2, v3
	s_cbranch_scc1 .LBB0_563
	v_readlane_b32 s0, v254, 32
	v_readlane_b32 s1, v254, 33
	v_readlane_b32 s2, v254, 30
	v_cvt_f32_u32_e32 v4, s0
	s_load_dwordx2 s[0:1], s[14:15], 0x80
	v_readlane_b32 s3, v254, 31
	s_and_b64 s[2:3], s[2:3], exec
	s_cselect_b32 s2, 0x200, 0
	v_add_f32_e32 v0, v0, v1
	s_waitcnt lgkmcnt(0)
	s_add_u32 s18, s0, s2
	s_addc_u32 s19, s1, 0
	v_readlane_b32 s2, v254, 39
	v_readlane_b32 s3, v254, 40
	s_add_u32 s0, s2, 0x4b400000
	v_writelane_b32 v254, s0, 50
	s_addc_u32 s0, s3, 0
	s_add_u32 s95, s2, 0x4f800000
	s_addc_u32 s96, s3, 0
	v_writelane_b32 v254, s0, 52
	s_add_u32 s97, s2, 0x53c00000
	s_addc_u32 s87, s3, 0
	v_readlane_b32 s4, v254, 48
	s_cmp_lt_i32 s4, 4
	s_cselect_b64 s[20:21], -1, 0
	s_cmp_gt_i32 s4, 3
	v_readlane_b32 s0, v254, 45
	s_cselect_b64 s[22:23], -1, 0
	s_and_b32 s14, s0, 48
	s_add_i32 s0, s79, 0x1000
	v_writelane_b32 v254, s0, 53
	s_lshr_b32 s0, s4, 2
	v_mul_f32_e32 v1, 0xbe99999a, v4
	v_add_f32_e32 v2, v2, v3
	s_cmp_eq_u32 s0, 0
	v_mul_f32_e32 v1, 0x3fb8aa3b, v1
	v_mul_f32_e32 v0, 0x3fb8aa3b, v0
	v_mul_f32_e32 v2, 0x3fb8aa3b, v2
	s_cselect_b64 s[24:25], -1, 0
	s_cmp_eq_u32 s0, 1
	v_exp_f32_e32 v1, v1
	v_exp_f32_e32 v0, v0
	v_exp_f32_e32 v2, v2
	s_cselect_b64 s[26:27], -1, 0
	s_add_i32 s76, s79, 0x3000
	v_readlane_b32 s0, v254, 11
	v_readlane_b32 s1, v254, 12
	s_add_u32 s0, s2, s0
	s_addc_u32 s1, s3, s1
	v_mov_b32_e32 v3, 0x3f4ccccd
	s_add_u32 s28, s0, 0x9d400000
	v_fmamk_f32 v1, v1, 0xbf19999a, v3
	v_sub_f32_e32 v0, v0, v2
	s_addc_u32 s29, s1, 0
	s_lshl_b32 s0, s4, 12
	v_add_f32_e32 v213, v1, v0
	v_sub_f32_e32 v214, 1.0, v1
	s_add_i32 s89, s91, s0
	v_readlane_b32 s8, v254, 37
	s_branch .LBB0_472
